# gating phase body hand-rewritten: U tiles prefetched two half-passes ahead in dedicated registers, SSQ sums deferred, gains hoisted
# speedup vs baseline: 1.0044x; 1.0044x over previous
.Lgt_new:
	s_and_b32 s0, s96, 7
	s_cmp_lg_u32 s0, 0
	s_cbranch_scc1 .Lgt_old
	s_cmpk_gt_u32 s88, 0x7ff
	s_cbranch_scc1 .LBB0_690
	v_readlane_b32 s0, v253, 0
	v_readlane_b32 s1, v253, 1
	s_nop 0
	s_load_dwordx2 s[4:5], s[0:1], 0xa0
	s_load_dwordx4 s[24:27], s[0:1], 0x28
	s_load_dwordx2 s[38:39], s[0:1], 0x38
	v_lshrrev_b32_e32 v238, 6, v0
	v_and_b32_e32 v235, 15, v0
	v_bfe_u32 v234, v0, 4, 2
	v_readfirstlane_b32 s17, v238
	v_lshlrev_b32_e32 v200, 2, v0
	v_cmp_gt_u32_e32 vcc, 0x80, v0
	s_and_b32 s8, s88, 7
	s_mov_b64 s[40:41], vcc
	v_mul_u32_u24_e32 v202, 0x110, v235
	v_lshl_add_u32 v202, v234, 4, v202
	v_mul_u32_u24_e32 v203, 0x610, v235
	v_lshl_add_u32 v203, v234, 4, v203
	s_mul_i32 s10, s17, 0xc0
	s_add_i32 s9, s10, 0xa000
	v_add_u32_e32 v203, s9, v203
	v_add_u32_e32 v204, 0xc200, v203
	v_lshlrev_b32_e32 v236, 4, v234
	v_add_u32_e32 v236, s10, v236
	v_lshlrev_b32_e32 v237, 2, v235
	v_lshlrev_b32_e32 v205, 8, v235
	v_lshl_add_u32 v205, v234, 4, v205
	s_mul_i32 s10, s17, 0x3000
	v_add_u32_e32 v205, s10, v205
	v_lshrrev_b32_e32 v206, 7, v0
	v_mul_u32_u24_e32 v206, 0xc0000, v206
	v_and_b32_e32 v238, 0x7f, v0
	v_lshl_add_u32 v206, v238, 2, v206
	v_lshlrev_b32_e32 v201, 5, v234
	v_lshrrev_b32_e32 v241, 5, v0
	v_mul_u32_u24_e32 v241, 0x110, v241
	v_and_b32_e32 v238, 31, v0
	v_lshl_add_u32 v241, v238, 3, v241
	v_lshlrev_b32_e32 v242, 4, v0
	v_mov_b32_e32 v238, v0
	v_mul_u32_u24_e32 v239, 0xaaab, v238
	v_lshrrev_b32_e32 v239, 21, v239
	v_mul_u32_u24_e32 v240, 48, v239
	v_sub_u32_e32 v240, v238, v240
	v_mul_u32_u24_e32 v228, 0x1800, v239
	v_lshl_add_u32 v228, v240, 4, v228
	v_mul_u32_u24_e32 v211, 0x610, v239
	v_lshl_add_u32 v211, v240, 5, v211
	v_add_u32_e32 v211, 0xa000, v211
	v_add_u32_e32 v238, 0x200, v0
	v_mul_u32_u24_e32 v239, 0xaaab, v238
	v_lshrrev_b32_e32 v239, 21, v239
	v_mul_u32_u24_e32 v240, 48, v239
	v_sub_u32_e32 v240, v238, v240
	v_mul_u32_u24_e32 v229, 0x1800, v239
	v_lshl_add_u32 v229, v240, 4, v229
	v_mul_u32_u24_e32 v213, 0x610, v239
	v_lshl_add_u32 v213, v240, 5, v213
	v_add_u32_e32 v213, 0xa000, v213
	v_add_u32_e32 v238, 0x400, v0
	v_mul_u32_u24_e32 v239, 0xaaab, v238
	v_lshrrev_b32_e32 v239, 21, v239
	v_mul_u32_u24_e32 v240, 48, v239
	v_sub_u32_e32 v240, v238, v240
	v_mul_u32_u24_e32 v230, 0x1800, v239
	v_lshl_add_u32 v230, v240, 4, v230
	v_mul_u32_u24_e32 v215, 0x610, v239
	v_lshl_add_u32 v215, v240, 5, v215
	v_add_u32_e32 v215, 0xa000, v215
	v_add_u32_e32 v238, 0x600, v0
	v_mul_u32_u24_e32 v239, 0xaaab, v238
	v_lshrrev_b32_e32 v239, 21, v239
	v_mul_u32_u24_e32 v240, 48, v239
	v_sub_u32_e32 v240, v238, v240
	v_mul_u32_u24_e32 v231, 0x1800, v239
	v_lshl_add_u32 v231, v240, 4, v231
	v_mul_u32_u24_e32 v217, 0x610, v239
	v_lshl_add_u32 v217, v240, 5, v217
	v_add_u32_e32 v217, 0xa000, v217
	v_add_u32_e32 v238, 0x800, v0
	v_mul_u32_u24_e32 v239, 0xaaab, v238
	v_lshrrev_b32_e32 v239, 21, v239
	v_mul_u32_u24_e32 v240, 48, v239
	v_sub_u32_e32 v240, v238, v240
	v_mul_u32_u24_e32 v232, 0x1800, v239
	v_lshl_add_u32 v232, v240, 4, v232
	v_mul_u32_u24_e32 v219, 0x610, v239
	v_lshl_add_u32 v219, v240, 5, v219
	v_add_u32_e32 v219, 0xa000, v219
	v_add_u32_e32 v238, 0xa00, v0
	v_mul_u32_u24_e32 v239, 0xaaab, v238
	v_lshrrev_b32_e32 v239, 21, v239
	v_mul_u32_u24_e32 v240, 48, v239
	v_sub_u32_e32 v240, v238, v240
	v_mul_u32_u24_e32 v233, 0x1800, v239
	v_lshl_add_u32 v233, v240, 4, v233
	v_mul_u32_u24_e32 v221, 0x610, v239
	v_lshl_add_u32 v221, v240, 5, v221
	v_add_u32_e32 v221, 0xa000, v221
	s_waitcnt lgkmcnt(0)
	s_add_u32 s12, s4, 0x4be00000
	s_addc_u32 s13, s5, 0
	s_mul_i32 s10, s8, 0x18000
	s_add_u32 s12, s12, s10
	s_addc_u32 s13, s13, 0
	s_add_u32 s14, s4, 0x57e00000
	s_addc_u32 s15, s5, 0
	s_mul_i32 s10, s8, 0x300
	s_add_u32 s6, s4, 0x58200000
	s_addc_u32 s7, s5, 0
	s_add_u32 s6, s6, s10
	s_addc_u32 s7, s7, 0
	s_add_u32 s4, s4, 0x3fe00000
	s_addc_u32 s5, s5, 0
	s_add_u32 s4, s4, s10
	s_addc_u32 s5, s5, 0
	s_lshl_b32 s10, s28, 19
	s_lshl_b32 s9, s8, 16
	s_add_u32 s26, s26, s10
	s_addc_u32 s27, s27, 0
	s_add_u32 s26, s26, s9
	s_addc_u32 s27, s27, 0
	global_load_dwordx4 v[50:53], v242, s[26:27]
	s_add_u32 s26, s26, 0x2000
	s_addc_u32 s27, s27, 0
	global_load_dwordx4 v[54:57], v242, s[26:27]
	s_add_u32 s26, s26, 0x2000
	s_addc_u32 s27, s27, 0
	global_load_dwordx4 v[58:61], v242, s[26:27]
	s_add_u32 s26, s26, 0x2000
	s_addc_u32 s27, s27, 0
	global_load_dwordx4 v[62:65], v242, s[26:27]
	s_add_u32 s26, s26, 0x2000
	s_addc_u32 s27, s27, 0
	global_load_dwordx4 v[66:69], v242, s[26:27]
	s_add_u32 s26, s26, 0x2000
	s_addc_u32 s27, s27, 0
	global_load_dwordx4 v[70:73], v242, s[26:27]
	s_add_u32 s26, s26, 0x2000
	s_addc_u32 s27, s27, 0
	global_load_dwordx4 v[74:77], v242, s[26:27]
	s_add_u32 s26, s26, 0x2000
	s_addc_u32 s27, s27, 0
	global_load_dwordx4 v[78:81], v242, s[26:27]
	s_mul_i32 s10, s28, 0x3000
	s_mul_i32 s9, s8, 0x600
	s_add_u32 s24, s24, s10
	s_addc_u32 s25, s25, 0
	s_add_u32 s24, s24, s9
	s_addc_u32 s25, s25, 0
	global_load_dwordx4 v[168:171], v236, s[24:25]
	global_load_dwordx4 v[172:175], v236, s[24:25] offset:64
	global_load_dwordx4 v[176:179], v236, s[24:25] offset:128
	s_lshl_b32 s10, s28, 12
	s_lshl_b32 s9, s8, 9
	s_add_u32 s38, s38, s10
	s_addc_u32 s39, s39, 0
	s_add_u32 s38, s38, s9
	s_addc_u32 s39, s39, 0
	global_load_dword v210, v237, s[38:39]
	global_load_dword v212, v237, s[38:39] offset:64
	global_load_dword v214, v237, s[38:39] offset:128
	global_load_dword v216, v237, s[38:39] offset:192
	global_load_dword v218, v237, s[38:39] offset:256
	global_load_dword v220, v237, s[38:39] offset:320
	global_load_dword v222, v237, s[38:39] offset:384
	global_load_dword v224, v237, s[38:39] offset:448
	s_mov_b32 s16, s88
	s_lshr_b32 s8, s16, 3
	s_mul_i32 s10, s8, 0xc0000
	s_add_u32 s24, s4, s10
	s_addc_u32 s25, s5, 0
	global_load_dwordx4 v[114:117], v228, s[24:25] nt
	global_load_dwordx4 v[118:121], v229, s[24:25] nt
	global_load_dwordx4 v[122:125], v230, s[24:25] nt
	global_load_dwordx4 v[126:129], v231, s[24:25] nt
	global_load_dwordx4 v[130:133], v232, s[24:25] nt
	global_load_dwordx4 v[134:137], v233, s[24:25] nt
	s_mul_i32 s10, s8, 0xc0000
	s_add_u32 s38, s12, s10
	s_addc_u32 s39, s13, 0
	global_load_dwordx4 v[2:5], v205, s[38:39] nt
	global_load_dwordx4 v[6:9], v205, s[38:39] offset:64 nt
	global_load_dwordx4 v[10:13], v205, s[38:39] offset:128 nt
	global_load_dwordx4 v[14:17], v205, s[38:39] offset:192 nt
	s_add_u32 s38, s38, 0x1000
	s_addc_u32 s39, s39, 0
	global_load_dwordx4 v[18:21], v205, s[38:39] nt
	global_load_dwordx4 v[22:25], v205, s[38:39] offset:64 nt
	global_load_dwordx4 v[26:29], v205, s[38:39] offset:128 nt
	global_load_dwordx4 v[30:33], v205, s[38:39] offset:192 nt
	s_add_u32 s38, s38, 0x1000
	s_addc_u32 s39, s39, 0
	global_load_dwordx4 v[34:37], v205, s[38:39] nt
	global_load_dwordx4 v[38:41], v205, s[38:39] offset:64 nt
	global_load_dwordx4 v[42:45], v205, s[38:39] offset:128 nt
	global_load_dwordx4 v[46:49], v205, s[38:39] offset:192 nt
	s_lshl_b32 s10, s8, 9
	s_add_u32 s38, s14, s10
	s_addc_u32 s39, s15, 0
	global_load_dword v162, v206, s[38:39]
	s_add_u32 s38, s38, 0x20000
	s_addc_u32 s39, s39, 0
	global_load_dword v163, v206, s[38:39]
	s_add_u32 s38, s38, 0x20000
	s_addc_u32 s39, s39, 0
	global_load_dword v164, v206, s[38:39]
	s_add_u32 s38, s38, 0x20000
	s_addc_u32 s39, s39, 0
	global_load_dword v165, v206, s[38:39]
	s_add_u32 s38, s38, 0x20000
	s_addc_u32 s39, s39, 0
	global_load_dword v166, v206, s[38:39]
	s_add_u32 s38, s38, 0x20000
	s_addc_u32 s39, s39, 0
	global_load_dword v167, v206, s[38:39]
	s_add_u32 s24, s24, 0x60000
	s_addc_u32 s25, s25, 0
	global_load_dwordx4 v[138:141], v228, s[24:25] nt
	global_load_dwordx4 v[142:145], v229, s[24:25] nt
	global_load_dwordx4 v[146:149], v230, s[24:25] nt
	global_load_dwordx4 v[150:153], v231, s[24:25] nt
	global_load_dwordx4 v[154:157], v232, s[24:25] nt
	global_load_dwordx4 v[158:161], v233, s[24:25] nt
	s_waitcnt vmcnt(41)
	v_cvt_pk_bf16_f32 v50, v50, v51
	v_cvt_pk_bf16_f32 v51, v52, v53
	s_nop 0
	ds_write_b64 v241, v[50:51]
	v_cvt_pk_bf16_f32 v54, v54, v55
	v_cvt_pk_bf16_f32 v55, v56, v57
	s_nop 0
	ds_write_b64 v241, v[54:55] offset:4352
	v_cvt_pk_bf16_f32 v58, v58, v59
	v_cvt_pk_bf16_f32 v59, v60, v61
	s_nop 0
	ds_write_b64 v241, v[58:59] offset:8704
	v_cvt_pk_bf16_f32 v62, v62, v63
	v_cvt_pk_bf16_f32 v63, v64, v65
	s_nop 0
	ds_write_b64 v241, v[62:63] offset:13056
	v_cvt_pk_bf16_f32 v66, v66, v67
	v_cvt_pk_bf16_f32 v67, v68, v69
	s_nop 0
	ds_write_b64 v241, v[66:67] offset:17408
	v_cvt_pk_bf16_f32 v70, v70, v71
	v_cvt_pk_bf16_f32 v71, v72, v73
	s_nop 0
	ds_write_b64 v241, v[70:71] offset:21760
	v_cvt_pk_bf16_f32 v74, v74, v75
	v_cvt_pk_bf16_f32 v75, v76, v77
	s_nop 0
	ds_write_b64 v241, v[74:75] offset:26112
	v_cvt_pk_bf16_f32 v78, v78, v79
	v_cvt_pk_bf16_f32 v79, v80, v81
	s_nop 0
	ds_write_b64 v241, v[78:79] offset:30464
	s_waitcnt vmcnt(6)
.Lgt_top:
	s_add_i32 s9, s16, s96
	s_cmpk_lt_u32 s9, 0x800
	s_cselect_b64 s[46:47], -1, 0
	s_waitcnt vmcnt(12)
	v_add_f32_e32 v196, v162, v163
	v_add_f32_e32 v196, v196, v164
	v_add_f32_e32 v196, v196, v165
	v_add_f32_e32 v196, v196, v166
	v_add_f32_e32 v196, v196, v167
	ds_write_b32 v200, v196 offset:37888
	s_waitcnt lgkmcnt(0)
	s_barrier
	s_and_saveexec_b64 s[44:45], s[40:41]
	s_cbranch_execz .Lgt_nr
	ds_read_b32 v196, v200 offset:37888
	ds_read_b32 v197, v200 offset:38400
	ds_read_b32 v198, v200 offset:38912
	ds_read_b32 v199, v200 offset:39424
	s_waitcnt lgkmcnt(2)
	v_add_f32_e32 v196, v196, v197
	s_waitcnt lgkmcnt(0)
	v_add_f32_e32 v198, v198, v199
	v_add_f32_e32 v196, v196, v198
	v_add_f32_e32 v196, 0x3b49539c, v196
	v_mul_f32_e32 v196, 0x39aaaaab, v196
	v_rsq_f32_e32 v196, v196
	s_nop 1
	ds_write_b32 v200, v196 offset:36864
.Lgt_nr:
	s_or_b64 exec, exec, s[44:45]
	s_waitcnt lgkmcnt(0)
	s_barrier
	ds_read_b128 v[180:183], v201 offset:36864
	ds_read_b128 v[184:187], v201 offset:36880
	ds_read_b128 v[188:191], v201 offset:36992
	ds_read_b128 v[192:195], v201 offset:37008
	s_waitcnt lgkmcnt(2)
	v_lshlrev_b32_e32 v196, 16, v2
	v_and_b32_e32 v197, 0xffff0000, v2
	v_lshlrev_b32_e32 v198, 16, v3
	v_and_b32_e32 v199, 0xffff0000, v3
	v_pk_mul_f32 v[196:197], v[180:181], v[196:197]
	v_pk_mul_f32 v[198:199], v[182:183], v[198:199]
	s_nop 0
	v_cvt_pk_bf16_f32 v2, v196, v197
	v_cvt_pk_bf16_f32 v3, v198, v199
	v_lshlrev_b32_e32 v196, 16, v4
	v_and_b32_e32 v197, 0xffff0000, v4
	v_lshlrev_b32_e32 v198, 16, v5
	v_and_b32_e32 v199, 0xffff0000, v5
	v_pk_mul_f32 v[196:197], v[184:185], v[196:197]
	v_pk_mul_f32 v[198:199], v[186:187], v[198:199]
	s_nop 0
	v_cvt_pk_bf16_f32 v4, v196, v197
	v_cvt_pk_bf16_f32 v5, v198, v199
	v_lshlrev_b32_e32 v196, 16, v18
	v_and_b32_e32 v197, 0xffff0000, v18
	v_lshlrev_b32_e32 v198, 16, v19
	v_and_b32_e32 v199, 0xffff0000, v19
	v_pk_mul_f32 v[196:197], v[180:181], v[196:197]
	v_pk_mul_f32 v[198:199], v[182:183], v[198:199]
	s_nop 0
	v_cvt_pk_bf16_f32 v18, v196, v197
	v_cvt_pk_bf16_f32 v19, v198, v199
	v_lshlrev_b32_e32 v196, 16, v20
	v_and_b32_e32 v197, 0xffff0000, v20
	v_lshlrev_b32_e32 v198, 16, v21
	v_and_b32_e32 v199, 0xffff0000, v21
	v_pk_mul_f32 v[196:197], v[184:185], v[196:197]
	v_pk_mul_f32 v[198:199], v[186:187], v[198:199]
	s_nop 0
	v_cvt_pk_bf16_f32 v20, v196, v197
	v_cvt_pk_bf16_f32 v21, v198, v199
	v_lshlrev_b32_e32 v196, 16, v34
	v_and_b32_e32 v197, 0xffff0000, v34
	v_lshlrev_b32_e32 v198, 16, v35
	v_and_b32_e32 v199, 0xffff0000, v35
	v_pk_mul_f32 v[196:197], v[180:181], v[196:197]
	v_pk_mul_f32 v[198:199], v[182:183], v[198:199]
	s_nop 0
	v_cvt_pk_bf16_f32 v34, v196, v197
	v_cvt_pk_bf16_f32 v35, v198, v199
	v_lshlrev_b32_e32 v196, 16, v36
	v_and_b32_e32 v197, 0xffff0000, v36
	v_lshlrev_b32_e32 v198, 16, v37
	v_and_b32_e32 v199, 0xffff0000, v37
	v_pk_mul_f32 v[196:197], v[184:185], v[196:197]
	v_pk_mul_f32 v[198:199], v[186:187], v[198:199]
	s_nop 0
	v_cvt_pk_bf16_f32 v36, v196, v197
	v_cvt_pk_bf16_f32 v37, v198, v199
	ds_read_b128 v[180:183], v201 offset:37120
	ds_read_b128 v[184:187], v201 offset:37136
	s_waitcnt lgkmcnt(2)
	v_lshlrev_b32_e32 v196, 16, v6
	v_and_b32_e32 v197, 0xffff0000, v6
	v_lshlrev_b32_e32 v198, 16, v7
	v_and_b32_e32 v199, 0xffff0000, v7
	v_pk_mul_f32 v[196:197], v[188:189], v[196:197]
	v_pk_mul_f32 v[198:199], v[190:191], v[198:199]
	s_nop 0
	v_cvt_pk_bf16_f32 v6, v196, v197
	v_cvt_pk_bf16_f32 v7, v198, v199
	v_lshlrev_b32_e32 v196, 16, v8
	v_and_b32_e32 v197, 0xffff0000, v8
	v_lshlrev_b32_e32 v198, 16, v9
	v_and_b32_e32 v199, 0xffff0000, v9
	v_pk_mul_f32 v[196:197], v[192:193], v[196:197]
	v_pk_mul_f32 v[198:199], v[194:195], v[198:199]
	s_nop 0
	v_cvt_pk_bf16_f32 v8, v196, v197
	v_cvt_pk_bf16_f32 v9, v198, v199
	v_lshlrev_b32_e32 v196, 16, v22
	v_and_b32_e32 v197, 0xffff0000, v22
	v_lshlrev_b32_e32 v198, 16, v23
	v_and_b32_e32 v199, 0xffff0000, v23
	v_pk_mul_f32 v[196:197], v[188:189], v[196:197]
	v_pk_mul_f32 v[198:199], v[190:191], v[198:199]
	s_nop 0
	v_cvt_pk_bf16_f32 v22, v196, v197
	v_cvt_pk_bf16_f32 v23, v198, v199
	v_lshlrev_b32_e32 v196, 16, v24
	v_and_b32_e32 v197, 0xffff0000, v24
	v_lshlrev_b32_e32 v198, 16, v25
	v_and_b32_e32 v199, 0xffff0000, v25
	v_pk_mul_f32 v[196:197], v[192:193], v[196:197]
	v_pk_mul_f32 v[198:199], v[194:195], v[198:199]
	s_nop 0
	v_cvt_pk_bf16_f32 v24, v196, v197
	v_cvt_pk_bf16_f32 v25, v198, v199
	v_lshlrev_b32_e32 v196, 16, v38
	v_and_b32_e32 v197, 0xffff0000, v38
	v_lshlrev_b32_e32 v198, 16, v39
	v_and_b32_e32 v199, 0xffff0000, v39
	v_pk_mul_f32 v[196:197], v[188:189], v[196:197]
	v_pk_mul_f32 v[198:199], v[190:191], v[198:199]
	s_nop 0
	v_cvt_pk_bf16_f32 v38, v196, v197
	v_cvt_pk_bf16_f32 v39, v198, v199
	v_lshlrev_b32_e32 v196, 16, v40
	v_and_b32_e32 v197, 0xffff0000, v40
	v_lshlrev_b32_e32 v198, 16, v41
	v_and_b32_e32 v199, 0xffff0000, v41
	v_pk_mul_f32 v[196:197], v[192:193], v[196:197]
	v_pk_mul_f32 v[198:199], v[194:195], v[198:199]
	s_nop 0
	v_cvt_pk_bf16_f32 v40, v196, v197
	v_cvt_pk_bf16_f32 v41, v198, v199
	ds_read_b128 v[188:191], v201 offset:37248
	ds_read_b128 v[192:195], v201 offset:37264
	s_waitcnt lgkmcnt(2)
	v_lshlrev_b32_e32 v196, 16, v10
	v_and_b32_e32 v197, 0xffff0000, v10
	v_lshlrev_b32_e32 v198, 16, v11
	v_and_b32_e32 v199, 0xffff0000, v11
	v_pk_mul_f32 v[196:197], v[180:181], v[196:197]
	v_pk_mul_f32 v[198:199], v[182:183], v[198:199]
	s_nop 0
	v_cvt_pk_bf16_f32 v10, v196, v197
	v_cvt_pk_bf16_f32 v11, v198, v199
	v_lshlrev_b32_e32 v196, 16, v12
	v_and_b32_e32 v197, 0xffff0000, v12
	v_lshlrev_b32_e32 v198, 16, v13
	v_and_b32_e32 v199, 0xffff0000, v13
	v_pk_mul_f32 v[196:197], v[184:185], v[196:197]
	v_pk_mul_f32 v[198:199], v[186:187], v[198:199]
	s_nop 0
	v_cvt_pk_bf16_f32 v12, v196, v197
	v_cvt_pk_bf16_f32 v13, v198, v199
	v_lshlrev_b32_e32 v196, 16, v26
	v_and_b32_e32 v197, 0xffff0000, v26
	v_lshlrev_b32_e32 v198, 16, v27
	v_and_b32_e32 v199, 0xffff0000, v27
	v_pk_mul_f32 v[196:197], v[180:181], v[196:197]
	v_pk_mul_f32 v[198:199], v[182:183], v[198:199]
	s_nop 0
	v_cvt_pk_bf16_f32 v26, v196, v197
	v_cvt_pk_bf16_f32 v27, v198, v199
	v_lshlrev_b32_e32 v196, 16, v28
	v_and_b32_e32 v197, 0xffff0000, v28
	v_lshlrev_b32_e32 v198, 16, v29
	v_and_b32_e32 v199, 0xffff0000, v29
	v_pk_mul_f32 v[196:197], v[184:185], v[196:197]
	v_pk_mul_f32 v[198:199], v[186:187], v[198:199]
	s_nop 0
	v_cvt_pk_bf16_f32 v28, v196, v197
	v_cvt_pk_bf16_f32 v29, v198, v199
	v_lshlrev_b32_e32 v196, 16, v42
	v_and_b32_e32 v197, 0xffff0000, v42
	v_lshlrev_b32_e32 v198, 16, v43
	v_and_b32_e32 v199, 0xffff0000, v43
	v_pk_mul_f32 v[196:197], v[180:181], v[196:197]
	v_pk_mul_f32 v[198:199], v[182:183], v[198:199]
	s_nop 0
	v_cvt_pk_bf16_f32 v42, v196, v197
	v_cvt_pk_bf16_f32 v43, v198, v199
	v_lshlrev_b32_e32 v196, 16, v44
	v_and_b32_e32 v197, 0xffff0000, v44
	v_lshlrev_b32_e32 v198, 16, v45
	v_and_b32_e32 v199, 0xffff0000, v45
	v_pk_mul_f32 v[196:197], v[184:185], v[196:197]
	v_pk_mul_f32 v[198:199], v[186:187], v[198:199]
	s_nop 0
	v_cvt_pk_bf16_f32 v44, v196, v197
	v_cvt_pk_bf16_f32 v45, v198, v199
	s_waitcnt lgkmcnt(0)
	v_lshlrev_b32_e32 v196, 16, v14
	v_and_b32_e32 v197, 0xffff0000, v14
	v_lshlrev_b32_e32 v198, 16, v15
	v_and_b32_e32 v199, 0xffff0000, v15
	v_pk_mul_f32 v[196:197], v[188:189], v[196:197]
	v_pk_mul_f32 v[198:199], v[190:191], v[198:199]
	s_nop 0
	v_cvt_pk_bf16_f32 v14, v196, v197
	v_cvt_pk_bf16_f32 v15, v198, v199
	v_lshlrev_b32_e32 v196, 16, v16
	v_and_b32_e32 v197, 0xffff0000, v16
	v_lshlrev_b32_e32 v198, 16, v17
	v_and_b32_e32 v199, 0xffff0000, v17
	v_pk_mul_f32 v[196:197], v[192:193], v[196:197]
	v_pk_mul_f32 v[198:199], v[194:195], v[198:199]
	s_nop 0
	v_cvt_pk_bf16_f32 v16, v196, v197
	v_cvt_pk_bf16_f32 v17, v198, v199
	v_lshlrev_b32_e32 v196, 16, v30
	v_and_b32_e32 v197, 0xffff0000, v30
	v_lshlrev_b32_e32 v198, 16, v31
	v_and_b32_e32 v199, 0xffff0000, v31
	v_pk_mul_f32 v[196:197], v[188:189], v[196:197]
	v_pk_mul_f32 v[198:199], v[190:191], v[198:199]
	s_nop 0
	v_cvt_pk_bf16_f32 v30, v196, v197
	v_cvt_pk_bf16_f32 v31, v198, v199
	v_lshlrev_b32_e32 v196, 16, v32
	v_and_b32_e32 v197, 0xffff0000, v32
	v_lshlrev_b32_e32 v198, 16, v33
	v_and_b32_e32 v199, 0xffff0000, v33
	v_pk_mul_f32 v[196:197], v[192:193], v[196:197]
	v_pk_mul_f32 v[198:199], v[194:195], v[198:199]
	s_nop 0
	v_cvt_pk_bf16_f32 v32, v196, v197
	v_cvt_pk_bf16_f32 v33, v198, v199
	v_lshlrev_b32_e32 v196, 16, v46
	v_and_b32_e32 v197, 0xffff0000, v46
	v_lshlrev_b32_e32 v198, 16, v47
	v_and_b32_e32 v199, 0xffff0000, v47
	v_pk_mul_f32 v[196:197], v[188:189], v[196:197]
	v_pk_mul_f32 v[198:199], v[190:191], v[198:199]
	s_nop 0
	v_cvt_pk_bf16_f32 v46, v196, v197
	v_cvt_pk_bf16_f32 v47, v198, v199
	v_lshlrev_b32_e32 v196, 16, v48
	v_and_b32_e32 v197, 0xffff0000, v48
	v_lshlrev_b32_e32 v198, 16, v49
	v_and_b32_e32 v199, 0xffff0000, v49
	v_pk_mul_f32 v[196:197], v[192:193], v[196:197]
	v_pk_mul_f32 v[198:199], v[194:195], v[198:199]
	s_nop 0
	v_cvt_pk_bf16_f32 v48, v196, v197
	v_cvt_pk_bf16_f32 v49, v198, v199
	s_lshr_b32 s10, s16, 3
	s_mul_i32 s10, s10, 0xc0000
	s_add_u32 s26, s6, s10
	s_addc_u32 s27, s7, 0
	s_lshr_b32 s8, s9, 3
	s_mul_i32 s10, s8, 0xc0000
	s_add_u32 s24, s4, s10
	s_addc_u32 s25, s5, 0
	ds_read_b128 v[98:101], v202 offset:0
	ds_read_b128 v[102:105], v202 offset:64
	ds_read_b128 v[106:109], v202 offset:128
	ds_read_b128 v[110:113], v202 offset:192
	s_waitcnt lgkmcnt(3)
	v_mfma_f32_16x16x32_bf16 v[50:53], v[2:5], v[98:101], 0
	v_mfma_f32_16x16x32_bf16 v[54:57], v[18:21], v[98:101], 0
	v_mfma_f32_16x16x32_bf16 v[58:61], v[34:37], v[98:101], 0
	ds_read_b128 v[98:101], v202 offset:4352
	s_waitcnt lgkmcnt(3)
	v_mfma_f32_16x16x32_bf16 v[50:53], v[6:9], v[102:105], v[50:53]
	v_mfma_f32_16x16x32_bf16 v[54:57], v[22:25], v[102:105], v[54:57]
	v_mfma_f32_16x16x32_bf16 v[58:61], v[38:41], v[102:105], v[58:61]
	ds_read_b128 v[102:105], v202 offset:4416
	s_waitcnt lgkmcnt(3)
	v_mfma_f32_16x16x32_bf16 v[50:53], v[10:13], v[106:109], v[50:53]
	v_mfma_f32_16x16x32_bf16 v[54:57], v[26:29], v[106:109], v[54:57]
	v_mfma_f32_16x16x32_bf16 v[58:61], v[42:45], v[106:109], v[58:61]
	ds_read_b128 v[106:109], v202 offset:4480
	s_waitcnt lgkmcnt(3)
	v_mfma_f32_16x16x32_bf16 v[50:53], v[14:17], v[110:113], v[50:53]
	v_mfma_f32_16x16x32_bf16 v[54:57], v[30:33], v[110:113], v[54:57]
	v_mfma_f32_16x16x32_bf16 v[58:61], v[46:49], v[110:113], v[58:61]
	ds_read_b128 v[110:113], v202 offset:4544
	s_waitcnt lgkmcnt(3)
	v_mfma_f32_16x16x32_bf16 v[62:65], v[2:5], v[98:101], 0
	v_mfma_f32_16x16x32_bf16 v[66:69], v[18:21], v[98:101], 0
	v_mfma_f32_16x16x32_bf16 v[70:73], v[34:37], v[98:101], 0
	ds_read_b128 v[98:101], v202 offset:8704
	s_waitcnt lgkmcnt(3)
	v_mfma_f32_16x16x32_bf16 v[62:65], v[6:9], v[102:105], v[62:65]
	v_mfma_f32_16x16x32_bf16 v[66:69], v[22:25], v[102:105], v[66:69]
	v_mfma_f32_16x16x32_bf16 v[70:73], v[38:41], v[102:105], v[70:73]
	ds_read_b128 v[102:105], v202 offset:8768
	s_waitcnt lgkmcnt(3)
	v_mfma_f32_16x16x32_bf16 v[62:65], v[10:13], v[106:109], v[62:65]
	v_mfma_f32_16x16x32_bf16 v[66:69], v[26:29], v[106:109], v[66:69]
	v_mfma_f32_16x16x32_bf16 v[70:73], v[42:45], v[106:109], v[70:73]
	ds_read_b128 v[106:109], v202 offset:8832
	s_waitcnt lgkmcnt(3)
	v_mfma_f32_16x16x32_bf16 v[62:65], v[14:17], v[110:113], v[62:65]
	v_mfma_f32_16x16x32_bf16 v[66:69], v[30:33], v[110:113], v[66:69]
	v_mfma_f32_16x16x32_bf16 v[70:73], v[46:49], v[110:113], v[70:73]
	ds_read_b128 v[110:113], v202 offset:8896
	s_waitcnt lgkmcnt(3)
	v_mfma_f32_16x16x32_bf16 v[74:77], v[2:5], v[98:101], 0
	v_mfma_f32_16x16x32_bf16 v[78:81], v[18:21], v[98:101], 0
	v_mfma_f32_16x16x32_bf16 v[82:85], v[34:37], v[98:101], 0
	ds_read_b128 v[98:101], v202 offset:13056
	s_waitcnt lgkmcnt(3)
	v_mfma_f32_16x16x32_bf16 v[74:77], v[6:9], v[102:105], v[74:77]
	v_mfma_f32_16x16x32_bf16 v[78:81], v[22:25], v[102:105], v[78:81]
	v_mfma_f32_16x16x32_bf16 v[82:85], v[38:41], v[102:105], v[82:85]
	ds_read_b128 v[102:105], v202 offset:13120
	s_waitcnt lgkmcnt(3)
	v_mfma_f32_16x16x32_bf16 v[74:77], v[10:13], v[106:109], v[74:77]
	v_mfma_f32_16x16x32_bf16 v[78:81], v[26:29], v[106:109], v[78:81]
	v_mfma_f32_16x16x32_bf16 v[82:85], v[42:45], v[106:109], v[82:85]
	ds_read_b128 v[106:109], v202 offset:13184
	s_waitcnt lgkmcnt(3)
	v_mfma_f32_16x16x32_bf16 v[74:77], v[14:17], v[110:113], v[74:77]
	v_mfma_f32_16x16x32_bf16 v[78:81], v[30:33], v[110:113], v[78:81]
	v_mfma_f32_16x16x32_bf16 v[82:85], v[46:49], v[110:113], v[82:85]
	ds_read_b128 v[110:113], v202 offset:13248
	s_waitcnt lgkmcnt(3)
	v_mfma_f32_16x16x32_bf16 v[86:89], v[2:5], v[98:101], 0
	v_mfma_f32_16x16x32_bf16 v[90:93], v[18:21], v[98:101], 0
	v_mfma_f32_16x16x32_bf16 v[94:97], v[34:37], v[98:101], 0
	s_waitcnt lgkmcnt(2)
	v_mfma_f32_16x16x32_bf16 v[86:89], v[6:9], v[102:105], v[86:89]
	v_mfma_f32_16x16x32_bf16 v[90:93], v[22:25], v[102:105], v[90:93]
	v_mfma_f32_16x16x32_bf16 v[94:97], v[38:41], v[102:105], v[94:97]
	s_waitcnt lgkmcnt(1)
	v_mfma_f32_16x16x32_bf16 v[86:89], v[10:13], v[106:109], v[86:89]
	v_mfma_f32_16x16x32_bf16 v[90:93], v[26:29], v[106:109], v[90:93]
	v_mfma_f32_16x16x32_bf16 v[94:97], v[42:45], v[106:109], v[94:97]
	s_waitcnt lgkmcnt(0)
	v_mfma_f32_16x16x32_bf16 v[86:89], v[14:17], v[110:113], v[86:89]
	v_mfma_f32_16x16x32_bf16 v[90:93], v[30:33], v[110:113], v[90:93]
	v_mfma_f32_16x16x32_bf16 v[94:97], v[46:49], v[110:113], v[94:97]
	v_pk_fma_f32 v[50:51], v[50:51], v[168:169], v[210:211] op_sel_hi:[1,1,0]
	v_pk_fma_f32 v[52:53], v[52:53], v[170:171], v[210:211] op_sel_hi:[1,1,0]
	v_pk_fma_f32 v[54:55], v[54:55], v[172:173], v[210:211] op_sel_hi:[1,1,0]
	v_pk_fma_f32 v[56:57], v[56:57], v[174:175], v[210:211] op_sel_hi:[1,1,0]
	ds_write_b128 v203, v[50:53] offset:0
	v_pk_fma_f32 v[58:59], v[58:59], v[176:177], v[210:211] op_sel_hi:[1,1,0]
	v_pk_fma_f32 v[60:61], v[60:61], v[178:179], v[210:211] op_sel_hi:[1,1,0]
	ds_write_b128 v203, v[54:57] offset:64
	v_pk_fma_f32 v[62:63], v[62:63], v[168:169], v[212:213] op_sel_hi:[1,1,0]
	v_pk_fma_f32 v[64:65], v[64:65], v[170:171], v[212:213] op_sel_hi:[1,1,0]
	ds_write_b128 v203, v[58:61] offset:128
	v_pk_fma_f32 v[66:67], v[66:67], v[172:173], v[212:213] op_sel_hi:[1,1,0]
	v_pk_fma_f32 v[68:69], v[68:69], v[174:175], v[212:213] op_sel_hi:[1,1,0]
	ds_write_b128 v203, v[62:65] offset:24832
	v_pk_fma_f32 v[70:71], v[70:71], v[176:177], v[212:213] op_sel_hi:[1,1,0]
	v_pk_fma_f32 v[72:73], v[72:73], v[178:179], v[212:213] op_sel_hi:[1,1,0]
	ds_write_b128 v203, v[66:69] offset:24896
	v_pk_fma_f32 v[74:75], v[74:75], v[168:169], v[214:215] op_sel_hi:[1,1,0]
	v_pk_fma_f32 v[76:77], v[76:77], v[170:171], v[214:215] op_sel_hi:[1,1,0]
	ds_write_b128 v203, v[70:73] offset:24960
	v_pk_fma_f32 v[78:79], v[78:79], v[172:173], v[214:215] op_sel_hi:[1,1,0]
	v_pk_fma_f32 v[80:81], v[80:81], v[174:175], v[214:215] op_sel_hi:[1,1,0]
	ds_write_b128 v204, v[74:77] offset:0
	v_pk_fma_f32 v[82:83], v[82:83], v[176:177], v[214:215] op_sel_hi:[1,1,0]
	v_pk_fma_f32 v[84:85], v[84:85], v[178:179], v[214:215] op_sel_hi:[1,1,0]
	ds_write_b128 v204, v[78:81] offset:64
	v_pk_fma_f32 v[86:87], v[86:87], v[168:169], v[216:217] op_sel_hi:[1,1,0]
	v_pk_fma_f32 v[88:89], v[88:89], v[170:171], v[216:217] op_sel_hi:[1,1,0]
	ds_write_b128 v204, v[82:85] offset:128
	v_pk_fma_f32 v[90:91], v[90:91], v[172:173], v[216:217] op_sel_hi:[1,1,0]
	v_pk_fma_f32 v[92:93], v[92:93], v[174:175], v[216:217] op_sel_hi:[1,1,0]
	ds_write_b128 v204, v[86:89] offset:24832
	v_pk_fma_f32 v[94:95], v[94:95], v[176:177], v[216:217] op_sel_hi:[1,1,0]
	v_pk_fma_f32 v[96:97], v[96:97], v[178:179], v[216:217] op_sel_hi:[1,1,0]
	ds_write_b128 v204, v[90:93] offset:24896
	s_nop 0
	ds_write_b128 v204, v[94:97] offset:24960
	s_waitcnt lgkmcnt(0)
	s_barrier
	s_and_b64 vcc, exec, s[46:47]
	ds_read_b128 v[180:183], v211
	ds_read_b128 v[184:187], v211 offset:16
	ds_read_b128 v[188:191], v213
	ds_read_b128 v[192:195], v213 offset:16
	s_waitcnt lgkmcnt(2)
	v_lshlrev_b32_e32 v196, 16, v114
	v_and_b32_e32 v197, 0xffff0000, v114
	v_lshlrev_b32_e32 v198, 16, v115
	v_and_b32_e32 v199, 0xffff0000, v115
	v_pk_mul_f32 v[180:181], v[180:181], v[196:197]
	v_pk_mul_f32 v[182:183], v[182:183], v[198:199]
	v_lshlrev_b32_e32 v196, 16, v116
	v_and_b32_e32 v197, 0xffff0000, v116
	v_lshlrev_b32_e32 v198, 16, v117
	v_and_b32_e32 v199, 0xffff0000, v117
	v_pk_mul_f32 v[184:185], v[184:185], v[196:197]
	v_pk_mul_f32 v[186:187], v[186:187], v[198:199]
	s_nop 0
	v_cvt_pk_bf16_f32 v180, v180, v181
	v_cvt_pk_bf16_f32 v181, v182, v183
	v_cvt_pk_bf16_f32 v182, v184, v185
	v_cvt_pk_bf16_f32 v183, v186, v187
	s_nop 0
	global_store_dwordx4 v228, v[180:183], s[26:27] nt
	s_cbranch_vccz .Lgt_nl0_0
	global_load_dwordx4 v[114:117], v228, s[24:25] nt
.Lgt_nl0_0:
	s_nop 0
	ds_read_b128 v[180:183], v215
	ds_read_b128 v[184:187], v215 offset:16
	s_waitcnt lgkmcnt(2)
	v_lshlrev_b32_e32 v196, 16, v118
	v_and_b32_e32 v197, 0xffff0000, v118
	v_lshlrev_b32_e32 v198, 16, v119
	v_and_b32_e32 v199, 0xffff0000, v119
	v_pk_mul_f32 v[188:189], v[188:189], v[196:197]
	v_pk_mul_f32 v[190:191], v[190:191], v[198:199]
	v_lshlrev_b32_e32 v196, 16, v120
	v_and_b32_e32 v197, 0xffff0000, v120
	v_lshlrev_b32_e32 v198, 16, v121
	v_and_b32_e32 v199, 0xffff0000, v121
	v_pk_mul_f32 v[192:193], v[192:193], v[196:197]
	v_pk_mul_f32 v[194:195], v[194:195], v[198:199]
	s_nop 0
	v_cvt_pk_bf16_f32 v188, v188, v189
	v_cvt_pk_bf16_f32 v189, v190, v191
	v_cvt_pk_bf16_f32 v190, v192, v193
	v_cvt_pk_bf16_f32 v191, v194, v195
	s_nop 0
	global_store_dwordx4 v229, v[188:191], s[26:27] nt
	s_cbranch_vccz .Lgt_nl0_1
	global_load_dwordx4 v[118:121], v229, s[24:25] nt
.Lgt_nl0_1:
	s_nop 0
	ds_read_b128 v[188:191], v217
	ds_read_b128 v[192:195], v217 offset:16
	s_waitcnt lgkmcnt(2)
	v_lshlrev_b32_e32 v196, 16, v122
	v_and_b32_e32 v197, 0xffff0000, v122
	v_lshlrev_b32_e32 v198, 16, v123
	v_and_b32_e32 v199, 0xffff0000, v123
	v_pk_mul_f32 v[180:181], v[180:181], v[196:197]
	v_pk_mul_f32 v[182:183], v[182:183], v[198:199]
	v_lshlrev_b32_e32 v196, 16, v124
	v_and_b32_e32 v197, 0xffff0000, v124
	v_lshlrev_b32_e32 v198, 16, v125
	v_and_b32_e32 v199, 0xffff0000, v125
	v_pk_mul_f32 v[184:185], v[184:185], v[196:197]
	v_pk_mul_f32 v[186:187], v[186:187], v[198:199]
	s_nop 0
	v_cvt_pk_bf16_f32 v180, v180, v181
	v_cvt_pk_bf16_f32 v181, v182, v183
	v_cvt_pk_bf16_f32 v182, v184, v185
	v_cvt_pk_bf16_f32 v183, v186, v187
	s_nop 0
	global_store_dwordx4 v230, v[180:183], s[26:27] nt
	s_cbranch_vccz .Lgt_nl0_2
	global_load_dwordx4 v[122:125], v230, s[24:25] nt
.Lgt_nl0_2:
	s_nop 0
	ds_read_b128 v[180:183], v219
	ds_read_b128 v[184:187], v219 offset:16
	s_waitcnt lgkmcnt(2)
	v_lshlrev_b32_e32 v196, 16, v126
	v_and_b32_e32 v197, 0xffff0000, v126
	v_lshlrev_b32_e32 v198, 16, v127
	v_and_b32_e32 v199, 0xffff0000, v127
	v_pk_mul_f32 v[188:189], v[188:189], v[196:197]
	v_pk_mul_f32 v[190:191], v[190:191], v[198:199]
	v_lshlrev_b32_e32 v196, 16, v128
	v_and_b32_e32 v197, 0xffff0000, v128
	v_lshlrev_b32_e32 v198, 16, v129
	v_and_b32_e32 v199, 0xffff0000, v129
	v_pk_mul_f32 v[192:193], v[192:193], v[196:197]
	v_pk_mul_f32 v[194:195], v[194:195], v[198:199]
	s_nop 0
	v_cvt_pk_bf16_f32 v188, v188, v189
	v_cvt_pk_bf16_f32 v189, v190, v191
	v_cvt_pk_bf16_f32 v190, v192, v193
	v_cvt_pk_bf16_f32 v191, v194, v195
	s_nop 0
	global_store_dwordx4 v231, v[188:191], s[26:27] nt
	s_cbranch_vccz .Lgt_nl0_3
	global_load_dwordx4 v[126:129], v231, s[24:25] nt
.Lgt_nl0_3:
	s_nop 0
	ds_read_b128 v[188:191], v221
	ds_read_b128 v[192:195], v221 offset:16
	s_waitcnt lgkmcnt(2)
	v_lshlrev_b32_e32 v196, 16, v130
	v_and_b32_e32 v197, 0xffff0000, v130
	v_lshlrev_b32_e32 v198, 16, v131
	v_and_b32_e32 v199, 0xffff0000, v131
	v_pk_mul_f32 v[180:181], v[180:181], v[196:197]
	v_pk_mul_f32 v[182:183], v[182:183], v[198:199]
	v_lshlrev_b32_e32 v196, 16, v132
	v_and_b32_e32 v197, 0xffff0000, v132
	v_lshlrev_b32_e32 v198, 16, v133
	v_and_b32_e32 v199, 0xffff0000, v133
	v_pk_mul_f32 v[184:185], v[184:185], v[196:197]
	v_pk_mul_f32 v[186:187], v[186:187], v[198:199]
	s_nop 0
	v_cvt_pk_bf16_f32 v180, v180, v181
	v_cvt_pk_bf16_f32 v181, v182, v183
	v_cvt_pk_bf16_f32 v182, v184, v185
	v_cvt_pk_bf16_f32 v183, v186, v187
	s_nop 0
	global_store_dwordx4 v232, v[180:183], s[26:27] nt
	s_cbranch_vccz .Lgt_nl0_4
	global_load_dwordx4 v[130:133], v232, s[24:25] nt
.Lgt_nl0_4:
	s_nop 0
	s_waitcnt lgkmcnt(0)
	v_lshlrev_b32_e32 v196, 16, v134
	v_and_b32_e32 v197, 0xffff0000, v134
	v_lshlrev_b32_e32 v198, 16, v135
	v_and_b32_e32 v199, 0xffff0000, v135
	v_pk_mul_f32 v[188:189], v[188:189], v[196:197]
	v_pk_mul_f32 v[190:191], v[190:191], v[198:199]
	v_lshlrev_b32_e32 v196, 16, v136
	v_and_b32_e32 v197, 0xffff0000, v136
	v_lshlrev_b32_e32 v198, 16, v137
	v_and_b32_e32 v199, 0xffff0000, v137
	v_pk_mul_f32 v[192:193], v[192:193], v[196:197]
	v_pk_mul_f32 v[194:195], v[194:195], v[198:199]
	s_nop 0
	v_cvt_pk_bf16_f32 v188, v188, v189
	v_cvt_pk_bf16_f32 v189, v190, v191
	v_cvt_pk_bf16_f32 v190, v192, v193
	v_cvt_pk_bf16_f32 v191, v194, v195
	s_nop 0
	global_store_dwordx4 v233, v[188:191], s[26:27] nt
	s_cbranch_vccz .Lgt_nl0_5
	global_load_dwordx4 v[134:137], v233, s[24:25] nt
.Lgt_nl0_5:
	s_nop 0
	s_barrier
	s_add_u32 s26, s26, 0x60000
	s_addc_u32 s27, s27, 0
	s_add_u32 s24, s24, 0x60000
	s_addc_u32 s25, s25, 0
	ds_read_b128 v[98:101], v202 offset:17408
	ds_read_b128 v[102:105], v202 offset:17472
	ds_read_b128 v[106:109], v202 offset:17536
	ds_read_b128 v[110:113], v202 offset:17600
	s_waitcnt lgkmcnt(3)
	v_mfma_f32_16x16x32_bf16 v[50:53], v[2:5], v[98:101], 0
	v_mfma_f32_16x16x32_bf16 v[54:57], v[18:21], v[98:101], 0
	v_mfma_f32_16x16x32_bf16 v[58:61], v[34:37], v[98:101], 0
	ds_read_b128 v[98:101], v202 offset:21760
	s_waitcnt lgkmcnt(3)
	v_mfma_f32_16x16x32_bf16 v[50:53], v[6:9], v[102:105], v[50:53]
	v_mfma_f32_16x16x32_bf16 v[54:57], v[22:25], v[102:105], v[54:57]
	v_mfma_f32_16x16x32_bf16 v[58:61], v[38:41], v[102:105], v[58:61]
	ds_read_b128 v[102:105], v202 offset:21824
	s_waitcnt lgkmcnt(3)
	v_mfma_f32_16x16x32_bf16 v[50:53], v[10:13], v[106:109], v[50:53]
	v_mfma_f32_16x16x32_bf16 v[54:57], v[26:29], v[106:109], v[54:57]
	v_mfma_f32_16x16x32_bf16 v[58:61], v[42:45], v[106:109], v[58:61]
	ds_read_b128 v[106:109], v202 offset:21888
	s_waitcnt lgkmcnt(3)
	v_mfma_f32_16x16x32_bf16 v[50:53], v[14:17], v[110:113], v[50:53]
	v_mfma_f32_16x16x32_bf16 v[54:57], v[30:33], v[110:113], v[54:57]
	v_mfma_f32_16x16x32_bf16 v[58:61], v[46:49], v[110:113], v[58:61]
	ds_read_b128 v[110:113], v202 offset:21952
	s_waitcnt lgkmcnt(3)
	v_mfma_f32_16x16x32_bf16 v[62:65], v[2:5], v[98:101], 0
	v_mfma_f32_16x16x32_bf16 v[66:69], v[18:21], v[98:101], 0
	v_mfma_f32_16x16x32_bf16 v[70:73], v[34:37], v[98:101], 0
	ds_read_b128 v[98:101], v202 offset:26112
	s_waitcnt lgkmcnt(3)
	v_mfma_f32_16x16x32_bf16 v[62:65], v[6:9], v[102:105], v[62:65]
	v_mfma_f32_16x16x32_bf16 v[66:69], v[22:25], v[102:105], v[66:69]
	v_mfma_f32_16x16x32_bf16 v[70:73], v[38:41], v[102:105], v[70:73]
	ds_read_b128 v[102:105], v202 offset:26176
	s_waitcnt lgkmcnt(3)
	v_mfma_f32_16x16x32_bf16 v[62:65], v[10:13], v[106:109], v[62:65]
	v_mfma_f32_16x16x32_bf16 v[66:69], v[26:29], v[106:109], v[66:69]
	v_mfma_f32_16x16x32_bf16 v[70:73], v[42:45], v[106:109], v[70:73]
	ds_read_b128 v[106:109], v202 offset:26240
	s_waitcnt lgkmcnt(3)
	v_mfma_f32_16x16x32_bf16 v[62:65], v[14:17], v[110:113], v[62:65]
	v_mfma_f32_16x16x32_bf16 v[66:69], v[30:33], v[110:113], v[66:69]
	v_mfma_f32_16x16x32_bf16 v[70:73], v[46:49], v[110:113], v[70:73]
	ds_read_b128 v[110:113], v202 offset:26304
	s_waitcnt lgkmcnt(3)
	v_mfma_f32_16x16x32_bf16 v[74:77], v[2:5], v[98:101], 0
	v_mfma_f32_16x16x32_bf16 v[78:81], v[18:21], v[98:101], 0
	v_mfma_f32_16x16x32_bf16 v[82:85], v[34:37], v[98:101], 0
	ds_read_b128 v[98:101], v202 offset:30464
	s_waitcnt lgkmcnt(3)
	v_mfma_f32_16x16x32_bf16 v[74:77], v[6:9], v[102:105], v[74:77]
	v_mfma_f32_16x16x32_bf16 v[78:81], v[22:25], v[102:105], v[78:81]
	v_mfma_f32_16x16x32_bf16 v[82:85], v[38:41], v[102:105], v[82:85]
	ds_read_b128 v[102:105], v202 offset:30528
	s_waitcnt lgkmcnt(3)
	v_mfma_f32_16x16x32_bf16 v[74:77], v[10:13], v[106:109], v[74:77]
	v_mfma_f32_16x16x32_bf16 v[78:81], v[26:29], v[106:109], v[78:81]
	v_mfma_f32_16x16x32_bf16 v[82:85], v[42:45], v[106:109], v[82:85]
	ds_read_b128 v[106:109], v202 offset:30592
	s_waitcnt lgkmcnt(3)
	v_mfma_f32_16x16x32_bf16 v[74:77], v[14:17], v[110:113], v[74:77]
	v_mfma_f32_16x16x32_bf16 v[78:81], v[30:33], v[110:113], v[78:81]
	v_mfma_f32_16x16x32_bf16 v[82:85], v[46:49], v[110:113], v[82:85]
	ds_read_b128 v[110:113], v202 offset:30656
	s_waitcnt lgkmcnt(3)
	v_mfma_f32_16x16x32_bf16 v[86:89], v[2:5], v[98:101], 0
	v_mfma_f32_16x16x32_bf16 v[90:93], v[18:21], v[98:101], 0
	v_mfma_f32_16x16x32_bf16 v[94:97], v[34:37], v[98:101], 0
	s_waitcnt lgkmcnt(2)
	v_mfma_f32_16x16x32_bf16 v[86:89], v[6:9], v[102:105], v[86:89]
	v_mfma_f32_16x16x32_bf16 v[90:93], v[22:25], v[102:105], v[90:93]
	v_mfma_f32_16x16x32_bf16 v[94:97], v[38:41], v[102:105], v[94:97]
	s_waitcnt lgkmcnt(1)
	v_mfma_f32_16x16x32_bf16 v[86:89], v[10:13], v[106:109], v[86:89]
	v_mfma_f32_16x16x32_bf16 v[90:93], v[26:29], v[106:109], v[90:93]
	v_mfma_f32_16x16x32_bf16 v[94:97], v[42:45], v[106:109], v[94:97]
	s_waitcnt lgkmcnt(0)
	v_mfma_f32_16x16x32_bf16 v[86:89], v[14:17], v[110:113], v[86:89]
	v_mfma_f32_16x16x32_bf16 v[90:93], v[30:33], v[110:113], v[90:93]
	v_mfma_f32_16x16x32_bf16 v[94:97], v[46:49], v[110:113], v[94:97]
	s_and_b64 vcc, exec, s[46:47]
	s_cbranch_vccz .Lgt_noreq
	s_mul_i32 s10, s8, 0xc0000
	s_add_u32 s38, s12, s10
	s_addc_u32 s39, s13, 0
	global_load_dwordx4 v[2:5], v205, s[38:39] nt
	global_load_dwordx4 v[6:9], v205, s[38:39] offset:64 nt
	global_load_dwordx4 v[10:13], v205, s[38:39] offset:128 nt
	global_load_dwordx4 v[14:17], v205, s[38:39] offset:192 nt
	s_add_u32 s38, s38, 0x1000
	s_addc_u32 s39, s39, 0
	global_load_dwordx4 v[18:21], v205, s[38:39] nt
	global_load_dwordx4 v[22:25], v205, s[38:39] offset:64 nt
	global_load_dwordx4 v[26:29], v205, s[38:39] offset:128 nt
	global_load_dwordx4 v[30:33], v205, s[38:39] offset:192 nt
	s_add_u32 s38, s38, 0x1000
	s_addc_u32 s39, s39, 0
	global_load_dwordx4 v[34:37], v205, s[38:39] nt
	global_load_dwordx4 v[38:41], v205, s[38:39] offset:64 nt
	global_load_dwordx4 v[42:45], v205, s[38:39] offset:128 nt
	global_load_dwordx4 v[46:49], v205, s[38:39] offset:192 nt
	s_lshl_b32 s10, s8, 9
	s_add_u32 s38, s14, s10
	s_addc_u32 s39, s15, 0
	global_load_dword v162, v206, s[38:39]
	s_add_u32 s38, s38, 0x20000
	s_addc_u32 s39, s39, 0
	global_load_dword v163, v206, s[38:39]
	s_add_u32 s38, s38, 0x20000
	s_addc_u32 s39, s39, 0
	global_load_dword v164, v206, s[38:39]
	s_add_u32 s38, s38, 0x20000
	s_addc_u32 s39, s39, 0
	global_load_dword v165, v206, s[38:39]
	s_add_u32 s38, s38, 0x20000
	s_addc_u32 s39, s39, 0
	global_load_dword v166, v206, s[38:39]
	s_add_u32 s38, s38, 0x20000
	s_addc_u32 s39, s39, 0
	global_load_dword v167, v206, s[38:39]
.Lgt_noreq:
	v_pk_fma_f32 v[50:51], v[50:51], v[168:169], v[218:219] op_sel_hi:[1,1,0]
	v_pk_fma_f32 v[52:53], v[52:53], v[170:171], v[218:219] op_sel_hi:[1,1,0]
	v_pk_fma_f32 v[54:55], v[54:55], v[172:173], v[218:219] op_sel_hi:[1,1,0]
	v_pk_fma_f32 v[56:57], v[56:57], v[174:175], v[218:219] op_sel_hi:[1,1,0]
	ds_write_b128 v203, v[50:53] offset:0
	v_pk_fma_f32 v[58:59], v[58:59], v[176:177], v[218:219] op_sel_hi:[1,1,0]
	v_pk_fma_f32 v[60:61], v[60:61], v[178:179], v[218:219] op_sel_hi:[1,1,0]
	ds_write_b128 v203, v[54:57] offset:64
	v_pk_fma_f32 v[62:63], v[62:63], v[168:169], v[220:221] op_sel_hi:[1,1,0]
	v_pk_fma_f32 v[64:65], v[64:65], v[170:171], v[220:221] op_sel_hi:[1,1,0]
	ds_write_b128 v203, v[58:61] offset:128
	v_pk_fma_f32 v[66:67], v[66:67], v[172:173], v[220:221] op_sel_hi:[1,1,0]
	v_pk_fma_f32 v[68:69], v[68:69], v[174:175], v[220:221] op_sel_hi:[1,1,0]
	ds_write_b128 v203, v[62:65] offset:24832
	v_pk_fma_f32 v[70:71], v[70:71], v[176:177], v[220:221] op_sel_hi:[1,1,0]
	v_pk_fma_f32 v[72:73], v[72:73], v[178:179], v[220:221] op_sel_hi:[1,1,0]
	ds_write_b128 v203, v[66:69] offset:24896
	v_pk_fma_f32 v[74:75], v[74:75], v[168:169], v[222:223] op_sel_hi:[1,1,0]
	v_pk_fma_f32 v[76:77], v[76:77], v[170:171], v[222:223] op_sel_hi:[1,1,0]
	ds_write_b128 v203, v[70:73] offset:24960
	v_pk_fma_f32 v[78:79], v[78:79], v[172:173], v[222:223] op_sel_hi:[1,1,0]
	v_pk_fma_f32 v[80:81], v[80:81], v[174:175], v[222:223] op_sel_hi:[1,1,0]
	ds_write_b128 v204, v[74:77] offset:0
	v_pk_fma_f32 v[82:83], v[82:83], v[176:177], v[222:223] op_sel_hi:[1,1,0]
	v_pk_fma_f32 v[84:85], v[84:85], v[178:179], v[222:223] op_sel_hi:[1,1,0]
	ds_write_b128 v204, v[78:81] offset:64
	v_pk_fma_f32 v[86:87], v[86:87], v[168:169], v[224:225] op_sel_hi:[1,1,0]
	v_pk_fma_f32 v[88:89], v[88:89], v[170:171], v[224:225] op_sel_hi:[1,1,0]
	ds_write_b128 v204, v[82:85] offset:128
	v_pk_fma_f32 v[90:91], v[90:91], v[172:173], v[224:225] op_sel_hi:[1,1,0]
	v_pk_fma_f32 v[92:93], v[92:93], v[174:175], v[224:225] op_sel_hi:[1,1,0]
	ds_write_b128 v204, v[86:89] offset:24832
	v_pk_fma_f32 v[94:95], v[94:95], v[176:177], v[224:225] op_sel_hi:[1,1,0]
	v_pk_fma_f32 v[96:97], v[96:97], v[178:179], v[224:225] op_sel_hi:[1,1,0]
	ds_write_b128 v204, v[90:93] offset:24896
	s_nop 0
	ds_write_b128 v204, v[94:97] offset:24960
	s_waitcnt lgkmcnt(0)
	s_and_b64 vcc, exec, s[46:47]
	s_cbranch_vccz .Lgt_w6
	s_waitcnt vmcnt(30)
	s_branch .Lgt_wd
.Lgt_w6:
	s_waitcnt vmcnt(6)
.Lgt_wd:
	s_barrier
	s_and_b64 vcc, exec, s[46:47]
	ds_read_b128 v[180:183], v211
	ds_read_b128 v[184:187], v211 offset:16
	ds_read_b128 v[188:191], v213
	ds_read_b128 v[192:195], v213 offset:16
	s_waitcnt lgkmcnt(2)
	v_lshlrev_b32_e32 v196, 16, v138
	v_and_b32_e32 v197, 0xffff0000, v138
	v_lshlrev_b32_e32 v198, 16, v139
	v_and_b32_e32 v199, 0xffff0000, v139
	v_pk_mul_f32 v[180:181], v[180:181], v[196:197]
	v_pk_mul_f32 v[182:183], v[182:183], v[198:199]
	v_lshlrev_b32_e32 v196, 16, v140
	v_and_b32_e32 v197, 0xffff0000, v140
	v_lshlrev_b32_e32 v198, 16, v141
	v_and_b32_e32 v199, 0xffff0000, v141
	v_pk_mul_f32 v[184:185], v[184:185], v[196:197]
	v_pk_mul_f32 v[186:187], v[186:187], v[198:199]
	s_nop 0
	v_cvt_pk_bf16_f32 v180, v180, v181
	v_cvt_pk_bf16_f32 v181, v182, v183
	v_cvt_pk_bf16_f32 v182, v184, v185
	v_cvt_pk_bf16_f32 v183, v186, v187
	s_nop 0
	global_store_dwordx4 v228, v[180:183], s[26:27] nt
	s_cbranch_vccz .Lgt_nl1_0
	global_load_dwordx4 v[138:141], v228, s[24:25] nt
.Lgt_nl1_0:
	s_nop 0
	ds_read_b128 v[180:183], v215
	ds_read_b128 v[184:187], v215 offset:16
	s_waitcnt lgkmcnt(2)
	v_lshlrev_b32_e32 v196, 16, v142
	v_and_b32_e32 v197, 0xffff0000, v142
	v_lshlrev_b32_e32 v198, 16, v143
	v_and_b32_e32 v199, 0xffff0000, v143
	v_pk_mul_f32 v[188:189], v[188:189], v[196:197]
	v_pk_mul_f32 v[190:191], v[190:191], v[198:199]
	v_lshlrev_b32_e32 v196, 16, v144
	v_and_b32_e32 v197, 0xffff0000, v144
	v_lshlrev_b32_e32 v198, 16, v145
	v_and_b32_e32 v199, 0xffff0000, v145
	v_pk_mul_f32 v[192:193], v[192:193], v[196:197]
	v_pk_mul_f32 v[194:195], v[194:195], v[198:199]
	s_nop 0
	v_cvt_pk_bf16_f32 v188, v188, v189
	v_cvt_pk_bf16_f32 v189, v190, v191
	v_cvt_pk_bf16_f32 v190, v192, v193
	v_cvt_pk_bf16_f32 v191, v194, v195
	s_nop 0
	global_store_dwordx4 v229, v[188:191], s[26:27] nt
	s_cbranch_vccz .Lgt_nl1_1
	global_load_dwordx4 v[142:145], v229, s[24:25] nt
.Lgt_nl1_1:
	s_nop 0
	ds_read_b128 v[188:191], v217
	ds_read_b128 v[192:195], v217 offset:16
	s_waitcnt lgkmcnt(2)
	v_lshlrev_b32_e32 v196, 16, v146
	v_and_b32_e32 v197, 0xffff0000, v146
	v_lshlrev_b32_e32 v198, 16, v147
	v_and_b32_e32 v199, 0xffff0000, v147
	v_pk_mul_f32 v[180:181], v[180:181], v[196:197]
	v_pk_mul_f32 v[182:183], v[182:183], v[198:199]
	v_lshlrev_b32_e32 v196, 16, v148
	v_and_b32_e32 v197, 0xffff0000, v148
	v_lshlrev_b32_e32 v198, 16, v149
	v_and_b32_e32 v199, 0xffff0000, v149
	v_pk_mul_f32 v[184:185], v[184:185], v[196:197]
	v_pk_mul_f32 v[186:187], v[186:187], v[198:199]
	s_nop 0
	v_cvt_pk_bf16_f32 v180, v180, v181
	v_cvt_pk_bf16_f32 v181, v182, v183
	v_cvt_pk_bf16_f32 v182, v184, v185
	v_cvt_pk_bf16_f32 v183, v186, v187
	s_nop 0
	global_store_dwordx4 v230, v[180:183], s[26:27] nt
	s_cbranch_vccz .Lgt_nl1_2
	global_load_dwordx4 v[146:149], v230, s[24:25] nt
.Lgt_nl1_2:
	s_nop 0
	ds_read_b128 v[180:183], v219
	ds_read_b128 v[184:187], v219 offset:16
	s_waitcnt lgkmcnt(2)
	v_lshlrev_b32_e32 v196, 16, v150
	v_and_b32_e32 v197, 0xffff0000, v150
	v_lshlrev_b32_e32 v198, 16, v151
	v_and_b32_e32 v199, 0xffff0000, v151
	v_pk_mul_f32 v[188:189], v[188:189], v[196:197]
	v_pk_mul_f32 v[190:191], v[190:191], v[198:199]
	v_lshlrev_b32_e32 v196, 16, v152
	v_and_b32_e32 v197, 0xffff0000, v152
	v_lshlrev_b32_e32 v198, 16, v153
	v_and_b32_e32 v199, 0xffff0000, v153
	v_pk_mul_f32 v[192:193], v[192:193], v[196:197]
	v_pk_mul_f32 v[194:195], v[194:195], v[198:199]
	s_nop 0
	v_cvt_pk_bf16_f32 v188, v188, v189
	v_cvt_pk_bf16_f32 v189, v190, v191
	v_cvt_pk_bf16_f32 v190, v192, v193
	v_cvt_pk_bf16_f32 v191, v194, v195
	s_nop 0
	global_store_dwordx4 v231, v[188:191], s[26:27] nt
	s_cbranch_vccz .Lgt_nl1_3
	global_load_dwordx4 v[150:153], v231, s[24:25] nt
.Lgt_nl1_3:
	s_nop 0
	ds_read_b128 v[188:191], v221
	ds_read_b128 v[192:195], v221 offset:16
	s_waitcnt lgkmcnt(2)
	v_lshlrev_b32_e32 v196, 16, v154
	v_and_b32_e32 v197, 0xffff0000, v154
	v_lshlrev_b32_e32 v198, 16, v155
	v_and_b32_e32 v199, 0xffff0000, v155
	v_pk_mul_f32 v[180:181], v[180:181], v[196:197]
	v_pk_mul_f32 v[182:183], v[182:183], v[198:199]
	v_lshlrev_b32_e32 v196, 16, v156
	v_and_b32_e32 v197, 0xffff0000, v156
	v_lshlrev_b32_e32 v198, 16, v157
	v_and_b32_e32 v199, 0xffff0000, v157
	v_pk_mul_f32 v[184:185], v[184:185], v[196:197]
	v_pk_mul_f32 v[186:187], v[186:187], v[198:199]
	s_nop 0
	v_cvt_pk_bf16_f32 v180, v180, v181
	v_cvt_pk_bf16_f32 v181, v182, v183
	v_cvt_pk_bf16_f32 v182, v184, v185
	v_cvt_pk_bf16_f32 v183, v186, v187
	s_nop 0
	global_store_dwordx4 v232, v[180:183], s[26:27] nt
	s_cbranch_vccz .Lgt_nl1_4
	global_load_dwordx4 v[154:157], v232, s[24:25] nt
.Lgt_nl1_4:
	s_nop 0
	s_waitcnt lgkmcnt(0)
	v_lshlrev_b32_e32 v196, 16, v158
	v_and_b32_e32 v197, 0xffff0000, v158
	v_lshlrev_b32_e32 v198, 16, v159
	v_and_b32_e32 v199, 0xffff0000, v159
	v_pk_mul_f32 v[188:189], v[188:189], v[196:197]
	v_pk_mul_f32 v[190:191], v[190:191], v[198:199]
	v_lshlrev_b32_e32 v196, 16, v160
	v_and_b32_e32 v197, 0xffff0000, v160
	v_lshlrev_b32_e32 v198, 16, v161
	v_and_b32_e32 v199, 0xffff0000, v161
	v_pk_mul_f32 v[192:193], v[192:193], v[196:197]
	v_pk_mul_f32 v[194:195], v[194:195], v[198:199]
	s_nop 0
	v_cvt_pk_bf16_f32 v188, v188, v189
	v_cvt_pk_bf16_f32 v189, v190, v191
	v_cvt_pk_bf16_f32 v190, v192, v193
	v_cvt_pk_bf16_f32 v191, v194, v195
	s_nop 0
	global_store_dwordx4 v233, v[188:191], s[26:27] nt
	s_cbranch_vccz .Lgt_nl1_5
	global_load_dwordx4 v[158:161], v233, s[24:25] nt
.Lgt_nl1_5:
	s_nop 0
	s_mov_b32 s16, s9
	s_and_b64 vcc, exec, s[46:47]
	s_cbranch_vccnz .Lgt_top
	s_branch .LBB0_690
.Lgt_old:
	v_readlane_b32 s8, v253, 0
	v_readlane_b32 s9, v253, 1
	v_mov_b32_e32 v160, v0
	s_waitcnt lgkmcnt(0)
	s_load_dwordx2 s[6:7], s[8:9], 0xa0
	v_readfirstlane_b32 s0, v160
	s_ashr_i32 s14, s0, 6
	v_readlane_b32 s12, v254, 26
	v_bfe_u32 v54, v160, 4, 2
	s_waitcnt lgkmcnt(0)
	s_add_u32 s0, s6, 0x4be00000
	s_addc_u32 s1, s7, 0
	s_add_u32 s4, s6, 0x57e00000
	v_readlane_b32 s13, v254, 27
	v_ashrrev_i32_e32 v2, 7, v160
	v_and_b32_e32 v3, 0x7f, v160
	s_addc_u32 s5, s7, 0
	v_and_b32_e32 v161, 15, v160
	v_mov_b32_e32 v166, 0
	s_andn2_b64 vcc, exec, s[12:13]
	v_lshlrev_b32_e32 v206, 4, v54
	v_mul_lo_u32 v50, v2, 6
	v_lshlrev_b32_e32 v52, 2, v3
	s_cbranch_vccnz .LBB0_676
	s_mul_i32 s10, s88, 0x180
	v_or_b32_e32 v2, s10, v161
	v_mad_u64_u32 v[2:3], s[12:13], s14, 48, v[2:3]
	v_ashrrev_i32_e32 v3, 31, v2
	v_lshl_add_u64 v[4:5], s[0:1], 0, v[206:207]
	v_lshlrev_b64 v[2:3], 8, v[2:3]
	v_lshl_add_u64 v[22:23], v[4:5], 0, v[2:3]
	s_mov_b64 s[12:13], 0x1000
	s_movk_i32 s10, 0x2000
	v_lshl_add_u64 v[30:31], v[22:23], 0, s[12:13]
	v_add_co_u32_e32 v32, vcc, s10, v22
	s_mov_b64 s[12:13], 0x2000
	v_readlane_b32 s10, v255, 35
	v_lshl_add_u64 v[46:47], v[22:23], 0, s[12:13]
	s_add_u32 s12, s4, s10
	s_addc_u32 s13, s5, 0
	v_mov_b32_e32 v53, v207
	v_ashrrev_i32_e32 v51, 31, v50
	v_or_b32_e32 v48, 1, v50
	v_lshl_add_u64 v[42:43], s[12:13], 0, v[52:53]
	v_lshlrev_b64 v[44:45], 17, v[50:51]
	v_ashrrev_i32_e32 v49, 31, v48
	v_addc_co_u32_e32 v33, vcc, 0, v23, vcc
	v_lshl_add_u64 v[44:45], v[42:43], 0, v[44:45]
	v_lshlrev_b64 v[48:49], 17, v[48:49]
	s_mov_b32 s10, 0x40000
	v_lshl_add_u64 v[42:43], v[42:43], 0, v[48:49]
	v_add_co_u32_e32 v48, vcc, s10, v44
	global_load_dwordx4 v[2:5], v[22:23], off nt
	global_load_dwordx4 v[6:9], v[22:23], off offset:64 nt
	global_load_dwordx4 v[10:13], v[22:23], off offset:128 nt
	global_load_dwordx4 v[14:17], v[22:23], off offset:192 nt
	v_addc_co_u32_e32 v49, vcc, 0, v45, vcc
	v_add_co_u32_e32 v56, vcc, 0x60000, v44
	global_load_dwordx4 v[18:21], v[30:31], off offset:64 nt
	global_load_dwordx4 v[26:29], v[30:31], off offset:128 nt
	v_addc_co_u32_e32 v57, vcc, 0, v45, vcc
	global_load_dwordx4 v[22:25], v[32:33], off offset:-4096 nt
	global_load_dwordx4 v[34:37], v[32:33], off nt
	s_nop 0
	global_load_dwordx4 v[30:33], v[30:31], off offset:192 nt
	s_nop 0
	global_load_dwordx4 v[38:41], v[46:47], off offset:64 nt
	v_add_co_u32_e32 v58, vcc, 0x80000, v44
	s_nop 1
	v_addc_co_u32_e32 v59, vcc, 0, v45, vcc
	v_add_co_u32_e32 v60, vcc, 0xa0000, v44
	s_nop 1
	v_addc_co_u32_e32 v61, vcc, 0, v45, vcc
	global_load_dword v51, v[44:45], off
	global_load_dword v53, v[42:43], off
	global_load_dword v55, v[48:49], off
	s_nop 0
	global_load_dword v56, v[56:57], off
	s_nop 0
	global_load_dword v57, v[58:59], off
	s_nop 0
	global_load_dword v58, v[60:61], off
	global_load_dwordx4 v[42:45], v[46:47], off offset:128 nt
	s_nop 0
	global_load_dwordx4 v[46:49], v[46:47], off offset:192 nt
	s_waitcnt vmcnt(0)
	v_add_f32_e32 v51, 0, v51
	v_add_f32_e32 v51, v51, v53
	v_add_f32_e32 v51, v51, v55
	v_add_f32_e32 v51, v51, v56
	v_add_f32_e32 v51, v51, v57
	v_add_f32_e32 v166, v51, v58
